# baseline (speedup 1.0000x reference)
.LBB0_82:
	s_and_b32 s0, s2, 3
	s_lshl_b32 s0, s0, s4
	v_or3_b32 v13, v14, s0, v13
	s_ashr_i32 s0, s2, 1
	s_and_b32 s0, s0, -16
	v_lshrrev_b32_e32 v11, 3, v0
	v_lshl_add_u32 v13, v13, 7, s0
	v_and_or_b32 v14, v11, 15, v13
	v_mov_b32_e32 v16, s16
	v_mov_b32_e32 v17, s17
	v_ashrrev_i32_e32 v15, 31, v14
	v_lshl_add_u64 v[14:15], v[14:15], 2, v[16:17]
	global_load_dword v13, v[14:15], off
	s_lshl_b32 s4, s33, 5
	v_cmp_gt_u32_e32 vcc, 32, v0
	s_and_saveexec_b64 s[0:1], vcc
	v_mov_b32_e32 v14, 0x14a00
	v_lshl_add_u32 v14, v0, 2, v14
	v_mov_b32_e32 v15, 0
	ds_write_b32 v14, v15
	s_or_b64 exec, exec, s[0:1]
	v_and_b32_e32 v14, 15, v0
	v_bfe_u32 v15, v0, 4, 2
	v_lshrrev_b32_e32 v16, 6, v0
	v_lshlrev_b32_e32 v17, 5, v14
	v_lshl_add_u32 v17, v16, 3, v17
	v_add_lshl_u32 v17, v17, v15, 4
	v_add_u32_e32 v18, 0x2000, v17
	v_add_u32_e32 v19, 0x4000, v17
	v_add_u32_e32 v20, 0x6000, v17
	global_load_dwordx4 v[24:27], v17, s[34:35]
	global_load_dwordx4 v[28:31], v17, s[34:35] offset:64
	global_load_dwordx4 v[32:35], v18, s[34:35]
	global_load_dwordx4 v[36:39], v18, s[34:35] offset:64
	global_load_dwordx4 v[40:43], v19, s[34:35]
	global_load_dwordx4 v[44:47], v19, s[34:35] offset:64
	global_load_dwordx4 v[48:51], v20, s[34:35]
	global_load_dwordx4 v[52:55], v20, s[34:35] offset:64
	v_lshlrev_b32_e32 v21, 3, v16
	v_add_lshl_u32 v21, v21, v15, 11
	s_lshl_b32 s0, s33, 7
	v_lshl_add_u32 v22, v14, 2, s0
	v_add_u32_e32 v21, v21, v22
	v_add_u32_e32 v22, 0x2000, v21
	global_load_dword v60, v21, s[18:19]
	global_load_dword v61, v21, s[18:19] offset:512
	global_load_dword v62, v21, s[18:19] offset:1024
	global_load_dword v63, v21, s[18:19] offset:1536
	global_load_dword v64, v22, s[18:19]
	global_load_dword v65, v22, s[18:19] offset:512
	global_load_dword v66, v22, s[18:19] offset:1024
	global_load_dword v67, v22, s[18:19] offset:1536
	global_load_dword v68, v21, s[18:19] offset:64
	global_load_dword v69, v21, s[18:19] offset:576
	global_load_dword v70, v21, s[18:19] offset:1088
	global_load_dword v71, v21, s[18:19] offset:1600
	global_load_dword v72, v22, s[18:19] offset:64
	global_load_dword v73, v22, s[18:19] offset:576
	global_load_dword v74, v22, s[18:19] offset:1088
	global_load_dword v75, v22, s[18:19] offset:1600
	global_load_dword v76, v21, s[22:23]
	global_load_dword v77, v21, s[22:23] offset:512
	global_load_dword v78, v21, s[22:23] offset:1024
	global_load_dword v79, v21, s[22:23] offset:1536
	global_load_dword v80, v22, s[22:23]
	global_load_dword v81, v22, s[22:23] offset:512
	global_load_dword v82, v22, s[22:23] offset:1024
	global_load_dword v83, v22, s[22:23] offset:1536
	global_load_dword v84, v21, s[22:23] offset:64
	global_load_dword v85, v21, s[22:23] offset:576
	global_load_dword v86, v21, s[22:23] offset:1088
	global_load_dword v87, v21, s[22:23] offset:1600
	global_load_dword v88, v22, s[22:23] offset:64
	global_load_dword v89, v22, s[22:23] offset:576
	global_load_dword v90, v22, s[22:23] offset:1088
	global_load_dword v91, v22, s[22:23] offset:1600
	v_lshlrev_b32_e32 v23, 4, v0
	v_add_u32_e32 v56, 0x10000, v23
	s_waitcnt vmcnt(0)
	v_cvt_pk_f16_f32 v92, v24, v25
	v_cvt_pk_f16_f32 v93, v26, v27
	v_cvt_pk_f16_f32 v94, v28, v29
	v_cvt_pk_f16_f32 v95, v30, v31
	ds_write_b128 v23, v[92:95] offset:51712
	v_cvt_pk_f16_f32 v96, v32, v33
	v_cvt_pk_f16_f32 v97, v34, v35
	v_cvt_pk_f16_f32 v98, v36, v37
	v_cvt_pk_f16_f32 v99, v38, v39
	ds_write_b128 v23, v[96:99] offset:55808
	v_cvt_pk_f16_f32 v100, v40, v41
	v_cvt_pk_f16_f32 v101, v42, v43
	v_cvt_pk_f16_f32 v102, v44, v45
	v_cvt_pk_f16_f32 v103, v46, v47
	ds_write_b128 v23, v[100:103] offset:59904
	v_cvt_pk_f16_f32 v104, v48, v49
	v_cvt_pk_f16_f32 v105, v50, v51
	v_cvt_pk_f16_f32 v106, v52, v53
	v_cvt_pk_f16_f32 v107, v54, v55
	ds_write_b128 v23, v[104:107] offset:64000
	v_cvt_pk_f16_f32 v108, v60, v61
	v_cvt_pk_f16_f32 v109, v62, v63
	v_cvt_pk_f16_f32 v110, v64, v65
	v_cvt_pk_f16_f32 v111, v66, v67
	ds_write_b128 v56, v[108:111] offset:2560
	v_cvt_pk_f16_f32 v112, v68, v69
	v_cvt_pk_f16_f32 v113, v70, v71
	v_cvt_pk_f16_f32 v114, v72, v73
	v_cvt_pk_f16_f32 v115, v74, v75
	ds_write_b128 v56, v[112:115] offset:6656
	v_cvt_pk_f16_f32 v116, v76, v77
	v_cvt_pk_f16_f32 v117, v78, v79
	v_cvt_pk_f16_f32 v118, v80, v81
	v_cvt_pk_f16_f32 v119, v82, v83
	ds_write_b128 v56, v[116:119] offset:10752
	v_cvt_pk_f16_f32 v120, v84, v85
	v_cvt_pk_f16_f32 v121, v86, v87
	v_cvt_pk_f16_f32 v122, v88, v89
	v_cvt_pk_f16_f32 v123, v90, v91
	ds_write_b128 v56, v[120:123] offset:14848
	s_movk_i32 s0, 0x80
	v_cmp_gt_u32_e32 vcc, s0, v0
	s_and_saveexec_b64 s[0:1], vcc
	s_cbranch_execz .LBB0_86
	v_cvt_f16_f32_e32 v13, v13
	v_lshl_or_b32 v18, s2, 7, v0
	v_mov_b32_e32 v16, s28
	v_mov_b32_e32 v17, s29
	v_ashrrev_i32_e32 v19, 31, v18
	v_lshl_add_u64 v[16:17], v[18:19], 1, v[16:17]
	global_store_short v[16:17], v13, off
